# prologue de-serialisation: weight-quantisation tasks issue all 16 tile loads before the first wait (was two 8-load trips); on top of w_in 27 tiles + dt routine + interleaved wave index
# baseline (speedup 1.0000x reference)
.LBB0_150:
	global_load_dwordx4 v[52:55], v[46:47], off
	v_lshl_add_u64 v[48:49], v[46:47], 0, s[2:3]
	global_load_dwordx4 v[56:59], v[48:49], off
	v_lshl_add_u64 v[48:49], v[48:49], 0, s[2:3]
	global_load_dwordx4 v[60:63], v[48:49], off
	v_lshl_add_u64 v[48:49], v[48:49], 0, s[2:3]
	global_load_dwordx4 v[64:67], v[48:49], off
	v_lshl_add_u64 v[48:49], v[48:49], 0, s[2:3]
	global_load_dwordx4 v[68:71], v[48:49], off
	v_lshl_add_u64 v[48:49], v[48:49], 0, s[2:3]
	global_load_dwordx4 v[72:75], v[48:49], off
	v_lshl_add_u64 v[48:49], v[48:49], 0, s[2:3]
	global_load_dwordx4 v[76:79], v[48:49], off
	v_lshl_add_u64 v[48:49], v[48:49], 0, s[2:3]
	global_load_dwordx4 v[88:91], v[48:49], off
	v_lshl_add_u64 v[46:47], v[46:47], 0, s[0:1]
	global_load_dwordx4 v[132:135], v[46:47], off
	v_lshl_add_u64 v[164:165], v[46:47], 0, s[2:3]
	global_load_dwordx4 v[136:139], v[164:165], off
	v_lshl_add_u64 v[164:165], v[164:165], 0, s[2:3]
	global_load_dwordx4 v[140:143], v[164:165], off
	v_lshl_add_u64 v[164:165], v[164:165], 0, s[2:3]
	global_load_dwordx4 v[144:147], v[164:165], off
	v_lshl_add_u64 v[164:165], v[164:165], 0, s[2:3]
	global_load_dwordx4 v[148:151], v[164:165], off
	v_lshl_add_u64 v[164:165], v[164:165], 0, s[2:3]
	global_load_dwordx4 v[152:155], v[164:165], off
	v_lshl_add_u64 v[164:165], v[164:165], 0, s[2:3]
	global_load_dwordx4 v[156:159], v[164:165], off
	v_lshl_add_u64 v[164:165], v[164:165], 0, s[2:3]
	global_load_dwordx4 v[160:163], v[164:165], off
	v_lshl_add_u64 v[46:47], v[46:47], 0, s[0:1]
	v_add_u32_e32 v0, s4, v83
	v_add_u32_e32 v44, 0x2100, v0
	v_add_u32_e32 v48, 0x2108, v0
	v_add_u32_e32 v49, 0x4200, v0
	v_add_u32_e32 v80, 0x4208, v0
	v_add_u32_e32 v81, 0x6300, v0
	v_add_u32_e32 v87, 0x6308, v0
	v_add_u32_e32 v92, 0x8400, v0
	v_add_u32_e32 v93, 0x8408, v0
	v_add_u32_e32 v94, 0xa500, v0
	v_add_u32_e32 v95, 0xa508, v0
	v_add_u32_e32 v96, 0xc600, v0
	v_add_u32_e32 v97, 0xc608, v0
	v_add_u32_e32 v98, 0xe700, v0
	v_add_u32_e32 v99, 0xe708, v0
	s_waitcnt vmcnt(15)
	v_cndmask_b32_e64 v54, v54, 0, vcc
	v_cndmask_b32_e64 v53, v53, 0, vcc
	v_cndmask_b32_e64 v52, v52, 0, vcc
	v_cndmask_b32_e64 v55, v55, 0, vcc
	ds_write2_b32 v0, v52, v53 offset1:1
	ds_write2_b32 v0, v54, v55 offset0:2 offset1:3
	s_waitcnt vmcnt(14)
	v_cndmask_b32_e64 v52, v58, 0, vcc
	v_cndmask_b32_e64 v53, v57, 0, vcc
	v_cndmask_b32_e64 v54, v56, 0, vcc
	v_cndmask_b32_e64 v0, v59, 0, vcc
	ds_write2_b32 v44, v54, v53 offset1:1
	ds_write2_b32 v48, v52, v0 offset1:1
	s_waitcnt vmcnt(13)
	v_cndmask_b32_e64 v48, v61, 0, vcc
	v_cndmask_b32_e64 v52, v60, 0, vcc
	v_cndmask_b32_e64 v0, v63, 0, vcc
	v_cndmask_b32_e64 v44, v62, 0, vcc
	ds_write2_b32 v49, v52, v48 offset1:1
	ds_write2_b32 v80, v44, v0 offset1:1
	s_waitcnt vmcnt(12)
	v_cndmask_b32_e64 v48, v65, 0, vcc
	v_cndmask_b32_e64 v49, v64, 0, vcc
	v_cndmask_b32_e64 v0, v67, 0, vcc
	v_cndmask_b32_e64 v44, v66, 0, vcc
	ds_write2_b32 v81, v49, v48 offset1:1
	ds_write2_b32 v87, v44, v0 offset1:1
	s_waitcnt vmcnt(11)
	v_cndmask_b32_e64 v48, v69, 0, vcc
	v_cndmask_b32_e64 v49, v68, 0, vcc
	v_cndmask_b32_e64 v0, v71, 0, vcc
	v_cndmask_b32_e64 v44, v70, 0, vcc
	ds_write2_b32 v92, v49, v48 offset1:1
	ds_write2_b32 v93, v44, v0 offset1:1
	s_waitcnt vmcnt(10)
	v_cndmask_b32_e64 v48, v73, 0, vcc
	v_cndmask_b32_e64 v49, v72, 0, vcc
	v_cndmask_b32_e64 v0, v75, 0, vcc
	v_cndmask_b32_e64 v44, v74, 0, vcc
	ds_write2_b32 v94, v49, v48 offset1:1
	ds_write2_b32 v95, v44, v0 offset1:1
	s_waitcnt vmcnt(9)
	v_cndmask_b32_e64 v48, v77, 0, vcc
	v_cndmask_b32_e64 v49, v76, 0, vcc
	v_cndmask_b32_e64 v0, v79, 0, vcc
	v_cndmask_b32_e64 v44, v78, 0, vcc
	ds_write2_b32 v96, v49, v48 offset1:1
	ds_write2_b32 v97, v44, v0 offset1:1
	s_waitcnt vmcnt(8)
	v_cndmask_b32_e64 v48, v89, 0, vcc
	v_cndmask_b32_e64 v49, v88, 0, vcc
	v_cndmask_b32_e64 v0, v91, 0, vcc
	v_cndmask_b32_e64 v44, v90, 0, vcc
	ds_write2_b32 v98, v49, v48 offset1:1
	ds_write2_b32 v99, v44, v0 offset1:1
	s_add_i32 s4, s4, 0x10800
	v_add_u32_e32 v0, s4, v83
	v_add_u32_e32 v44, 0x2100, v0
	v_add_u32_e32 v48, 0x2108, v0
	v_add_u32_e32 v49, 0x4200, v0
	v_add_u32_e32 v80, 0x4208, v0
	v_add_u32_e32 v81, 0x6300, v0
	v_add_u32_e32 v87, 0x6308, v0
	v_add_u32_e32 v92, 0x8400, v0
	v_add_u32_e32 v93, 0x8408, v0
	v_add_u32_e32 v94, 0xa500, v0
	v_add_u32_e32 v95, 0xa508, v0
	v_add_u32_e32 v96, 0xc600, v0
	v_add_u32_e32 v97, 0xc608, v0
	v_add_u32_e32 v98, 0xe700, v0
	v_add_u32_e32 v99, 0xe708, v0
	s_waitcnt vmcnt(7)
	v_cndmask_b32_e64 v54, v134, 0, vcc
	v_cndmask_b32_e64 v53, v133, 0, vcc
	v_cndmask_b32_e64 v52, v132, 0, vcc
	v_cndmask_b32_e64 v55, v135, 0, vcc
	ds_write2_b32 v0, v52, v53 offset1:1
	ds_write2_b32 v0, v54, v55 offset0:2 offset1:3
	s_waitcnt vmcnt(6)
	v_cndmask_b32_e64 v52, v138, 0, vcc
	v_cndmask_b32_e64 v53, v137, 0, vcc
	v_cndmask_b32_e64 v54, v136, 0, vcc
	v_cndmask_b32_e64 v0, v139, 0, vcc
	ds_write2_b32 v44, v54, v53 offset1:1
	ds_write2_b32 v48, v52, v0 offset1:1
	s_waitcnt vmcnt(5)
	v_cndmask_b32_e64 v48, v141, 0, vcc
	v_cndmask_b32_e64 v52, v140, 0, vcc
	v_cndmask_b32_e64 v0, v143, 0, vcc
	v_cndmask_b32_e64 v44, v142, 0, vcc
	ds_write2_b32 v49, v52, v48 offset1:1
	ds_write2_b32 v80, v44, v0 offset1:1
	s_waitcnt vmcnt(4)
	v_cndmask_b32_e64 v48, v145, 0, vcc
	v_cndmask_b32_e64 v49, v144, 0, vcc
	v_cndmask_b32_e64 v0, v147, 0, vcc
	v_cndmask_b32_e64 v44, v146, 0, vcc
	ds_write2_b32 v81, v49, v48 offset1:1
	ds_write2_b32 v87, v44, v0 offset1:1
	s_waitcnt vmcnt(3)
	v_cndmask_b32_e64 v48, v149, 0, vcc
	v_cndmask_b32_e64 v49, v148, 0, vcc
	v_cndmask_b32_e64 v0, v151, 0, vcc
	v_cndmask_b32_e64 v44, v150, 0, vcc
	ds_write2_b32 v92, v49, v48 offset1:1
	ds_write2_b32 v93, v44, v0 offset1:1
	s_waitcnt vmcnt(2)
	v_cndmask_b32_e64 v48, v153, 0, vcc
	v_cndmask_b32_e64 v49, v152, 0, vcc
	v_cndmask_b32_e64 v0, v155, 0, vcc
	v_cndmask_b32_e64 v44, v154, 0, vcc
	ds_write2_b32 v94, v49, v48 offset1:1
	ds_write2_b32 v95, v44, v0 offset1:1
	s_waitcnt vmcnt(1)
	v_cndmask_b32_e64 v48, v157, 0, vcc
	v_cndmask_b32_e64 v49, v156, 0, vcc
	v_cndmask_b32_e64 v0, v159, 0, vcc
	v_cndmask_b32_e64 v44, v158, 0, vcc
	ds_write2_b32 v96, v49, v48 offset1:1
	ds_write2_b32 v97, v44, v0 offset1:1
	s_waitcnt vmcnt(0)
	v_cndmask_b32_e64 v48, v161, 0, vcc
	v_cndmask_b32_e64 v49, v160, 0, vcc
	v_cndmask_b32_e64 v0, v163, 0, vcc
	v_cndmask_b32_e64 v44, v162, 0, vcc
	ds_write2_b32 v98, v49, v48 offset1:1
	ds_write2_b32 v99, v44, v0 offset1:1
	s_add_i32 s4, s4, 0x10800
	s_cmp_eq_u32 s4, 0x21000
	s_mov_b32 s0, 1
	v_mov_b32_e32 v44, v45
	v_writelane_b32 v252, s0, 52
	s_mov_b32 s0, 0
	v_writelane_b32 v252, s0, 54
	s_movk_i32 s33, 0xffe0
	s_mov_b64 s[12:13], 0
	v_mov_b64_e32 v[70:71], v[44:45]
	s_waitcnt lgkmcnt(0)
	s_barrier
	s_branch .LBB0_167
